# V phase: the 8-step s_waitcnt lgkmcnt ladder of each arithmetic block reduced to two waits (the gathers were issued a whole sub-batch earlier)
# speedup vs baseline: 1.0005x; 1.0005x over previous
; template <int VVAR> __device__ __forceinline__ void peer_v_phase(LAS unsigned char* lds, int wave, int vcu, const unsigned char* __restrict__ VS_l, const unsigned* __restrict__ PW, bf16* __restrict__ Y) {
;     ...
; #pragma unroll 1
;     for (int it = 0; it < (VVAR == 5 ? 2 : 64); it += 2) {
;         V_HALF(pa, pb, it + 1);
;         V_HALF(pb, pa, it + 2);
.LBB0_956:
	s_and_b32 s8, s3, 0x78
	s_add_i32 s8, s8, s4
	s_ashr_i32 s9, s8, 31
	s_lshl_b64 s[10:11], s[8:9], 15
	s_add_u32 s10, s12, s10
	s_addc_u32 s11, s13, s11
	s_and_b32 s17, s16, 0x1000
	s_lshl_b32 s17, s17, 2
	s_add_u32 s10, s10, s17
	s_addc_u32 s11, s11, 0
	s_add_u32 s62, s10, s6
	s_addc_u32 s63, s11, s7
	s_add_u32 s64, s10, s14
	s_addc_u32 s65, s11, 0
	s_mov_b32 s17, s18
	s_nop 0
	global_load_dword v104, v2, s[62:63] offset:256
	global_load_dword v106, v2, s[62:63] offset:512
	global_load_dword v108, v2, s[62:63] offset:768
	global_load_dword v110, v2, s[62:63] offset:1024
	global_load_dword v112, v2, s[62:63] offset:1280
	global_load_dword v114, v2, s[62:63] offset:1536
	global_load_dword v98, v2, s[62:63] offset:1792
	global_load_dword v100, v2, s[62:63] offset:2048
	global_load_dword v116, v2, s[64:65] offset:-4096
	global_load_dword v102, v2, s[62:63] offset:2304
	global_load_dword v78, v2, s[62:63] offset:2560
	global_load_dword v80, v2, s[62:63] offset:2816
	global_load_dword v82, v2, s[62:63] offset:3072
	global_load_dword v84, v2, s[62:63] offset:3328
	global_load_dword v86, v2, s[62:63] offset:3584
	global_load_dword v88, v2, s[62:63] offset:3840
	global_load_dword v90, v2, s[64:65]
	global_load_dword v92, v2, s[64:65] offset:256
	global_load_dword v94, v2, s[64:65] offset:512
	global_load_dword v96, v2, s[64:65] offset:768
	global_load_dword v76, v2, s[64:65] offset:1024
	global_load_dword v77, v2, s[64:65] offset:1280
	global_load_dword v56, v2, s[64:65] offset:1536
	global_load_dword v57, v2, s[64:65] offset:1792
	global_load_dword v58, v2, s[64:65] offset:2048
	global_load_dword v59, v2, s[64:65] offset:2304
	global_load_dword v60, v2, s[64:65] offset:2560
	global_load_dword v61, v2, s[64:65] offset:2816
	global_load_dword v62, v2, s[64:65] offset:3072
	global_load_dword v63, v2, s[64:65] offset:3328
	global_load_dword v54, v2, s[64:65] offset:3584
	global_load_dword v55, v2, s[64:65] offset:3840
	s_waitcnt vmcnt(56)
	v_and_b32_e32 v9, 0x1fff8, v64
	v_and_b32_e32 v11, 0x1fff8, v66
	v_and_b32_e32 v13, 0x1fff8, v68
	v_and_b32_e32 v15, 0x1fff8, v70
	ds_read_b64 v[126:127], v9
	ds_read_b64 v[128:129], v11
	ds_read_b64 v[130:131], v13
	ds_read_b64 v[132:133], v15
	v_and_b32_e32 v9, 0x1fff8, v72
	v_and_b32_e32 v11, 0x1fff8, v74
	v_and_b32_e32 v13, 0x1fff8, v48
	v_and_b32_e32 v15, 0x1fff8, v50
	ds_read_b64 v[134:135], v9
	ds_read_b64 v[136:137], v11
	ds_read_b64 v[138:139], v13
	ds_read_b64 v[140:141], v15
	s_setprio 1
	s_waitcnt lgkmcnt(4)
	v_cvt_pk_f32_fp8_e32 v[142:143], v126
	v_cvt_pk_f32_fp8_sdwa v[144:145], v126 src0_sel:WORD_1
	v_cvt_pk_f32_fp8_e32 v[146:147], v127
	v_cvt_pk_f32_fp8_sdwa v[126:127], v127 src0_sel:WORD_1
	v_cvt_pk_f32_fp8_e32 v[148:149], v128
	v_cvt_pk_f32_fp8_sdwa v[150:151], v128 src0_sel:WORD_1
	v_cvt_pk_f32_fp8_e32 v[152:153], v129
	v_cvt_pk_f32_fp8_sdwa v[128:129], v129 src0_sel:WORD_1
	v_cvt_pk_f32_fp8_e32 v[154:155], v130
	v_cvt_pk_f32_fp8_sdwa v[156:157], v130 src0_sel:WORD_1
	v_cvt_pk_f32_fp8_e32 v[158:159], v131
	v_cvt_pk_f32_fp8_sdwa v[130:131], v131 src0_sel:WORD_1
	v_cvt_pk_f32_fp8_e32 v[160:161], v132
	v_cvt_pk_f32_fp8_sdwa v[162:163], v132 src0_sel:WORD_1
	v_cvt_pk_f32_fp8_e32 v[164:165], v133
	v_cvt_pk_f32_fp8_sdwa v[132:133], v133 src0_sel:WORD_1
	s_waitcnt lgkmcnt(0)
	v_cvt_pk_f32_fp8_e32 v[166:167], v134
	v_cvt_pk_f32_fp8_sdwa v[168:169], v134 src0_sel:WORD_1
	v_cvt_pk_f32_fp8_e32 v[170:171], v135
	v_cvt_pk_f32_fp8_sdwa v[134:135], v135 src0_sel:WORD_1
	v_cvt_pk_f32_fp8_e32 v[172:173], v136
	v_cvt_pk_f32_fp8_sdwa v[174:175], v136 src0_sel:WORD_1
	v_cvt_pk_f32_fp8_e32 v[176:177], v137
	v_cvt_pk_f32_fp8_sdwa v[136:137], v137 src0_sel:WORD_1
	v_cvt_pk_f32_fp8_e32 v[178:179], v138
	v_cvt_pk_f32_fp8_sdwa v[180:181], v138 src0_sel:WORD_1
	v_cvt_pk_f32_fp8_e32 v[182:183], v139
	v_cvt_pk_f32_fp8_sdwa v[138:139], v139 src0_sel:WORD_1
	v_cvt_pk_f32_fp8_e32 v[184:185], v140
	v_cvt_pk_f32_fp8_sdwa v[186:187], v140 src0_sel:WORD_1
	v_cvt_pk_f32_fp8_e32 v[188:189], v141
	v_cvt_pk_f32_fp8_sdwa v[140:141], v141 src0_sel:WORD_1
	s_setprio 0
	s_waitcnt vmcnt(48)
	v_and_b32_e32 v9, 0x1fff8, v52
	v_and_b32_e32 v11, 0x1fff8, v32
	v_and_b32_e32 v13, 0x1fff8, v34
	v_and_b32_e32 v15, 0x1fff8, v36
	ds_read_b64 v[190:191], v9
	ds_read_b64 v[192:193], v11
	ds_read_b64 v[194:195], v13
	ds_read_b64 v[196:197], v15
	v_and_b32_e32 v9, 0x1fff8, v38
	v_and_b32_e32 v11, 0x1fff8, v40
	v_and_b32_e32 v13, 0x1fff8, v42
	v_and_b32_e32 v15, 0x1fff8, v44
	ds_read_b64 v[198:199], v9
	ds_read_b64 v[200:201], v11
	ds_read_b64 v[202:203], v13
	ds_read_b64 v[204:205], v15
	s_setprio 1
	v_pk_fma_f32 v[118:119], v[142:143], v[64:65], v[118:119] op_sel_hi:[1,0,1]
	v_pk_fma_f32 v[122:123], v[144:145], v[64:65], v[122:123] op_sel_hi:[1,0,1]
	v_pk_fma_f32 v[120:121], v[146:147], v[64:65], v[120:121] op_sel_hi:[1,0,1]
	v_pk_fma_f32 v[64:65], v[126:127], v[64:65], v[124:125] op_sel_hi:[1,0,1]
	v_pk_fma_f32 v[118:119], v[148:149], v[66:67], v[118:119] op_sel_hi:[1,0,1]
	v_pk_fma_f32 v[122:123], v[150:151], v[66:67], v[122:123] op_sel_hi:[1,0,1]
	v_pk_fma_f32 v[120:121], v[152:153], v[66:67], v[120:121] op_sel_hi:[1,0,1]
	v_pk_fma_f32 v[64:65], v[128:129], v[66:67], v[64:65] op_sel_hi:[1,0,1]
	v_pk_fma_f32 v[118:119], v[154:155], v[68:69], v[118:119] op_sel_hi:[1,0,1]
	v_pk_fma_f32 v[122:123], v[156:157], v[68:69], v[122:123] op_sel_hi:[1,0,1]
	v_pk_fma_f32 v[120:121], v[158:159], v[68:69], v[120:121] op_sel_hi:[1,0,1]
	v_pk_fma_f32 v[64:65], v[130:131], v[68:69], v[64:65] op_sel_hi:[1,0,1]
	v_pk_fma_f32 v[118:119], v[160:161], v[70:71], v[118:119] op_sel_hi:[1,0,1]
	v_pk_fma_f32 v[122:123], v[162:163], v[70:71], v[122:123] op_sel_hi:[1,0,1]
	v_pk_fma_f32 v[120:121], v[164:165], v[70:71], v[120:121] op_sel_hi:[1,0,1]
	v_pk_fma_f32 v[64:65], v[132:133], v[70:71], v[64:65] op_sel_hi:[1,0,1]
	s_waitcnt lgkmcnt(4)
	v_cvt_pk_f32_fp8_e32 v[206:207], v190
	v_cvt_pk_f32_fp8_sdwa v[208:209], v190 src0_sel:WORD_1
	v_cvt_pk_f32_fp8_e32 v[210:211], v191
	v_cvt_pk_f32_fp8_sdwa v[190:191], v191 src0_sel:WORD_1
	v_pk_fma_f32 v[118:119], v[166:167], v[72:73], v[118:119] op_sel_hi:[1,0,1]
	v_pk_fma_f32 v[122:123], v[168:169], v[72:73], v[122:123] op_sel_hi:[1,0,1]
	v_pk_fma_f32 v[120:121], v[170:171], v[72:73], v[120:121] op_sel_hi:[1,0,1]
	v_pk_fma_f32 v[64:65], v[134:135], v[72:73], v[64:65] op_sel_hi:[1,0,1]
	v_pk_fma_f32 v[118:119], v[172:173], v[74:75], v[118:119] op_sel_hi:[1,0,1]
	v_pk_fma_f32 v[122:123], v[174:175], v[74:75], v[122:123] op_sel_hi:[1,0,1]
	v_pk_fma_f32 v[120:121], v[176:177], v[74:75], v[120:121] op_sel_hi:[1,0,1]
	v_pk_fma_f32 v[64:65], v[136:137], v[74:75], v[64:65] op_sel_hi:[1,0,1]
	v_cvt_pk_f32_fp8_e32 v[66:67], v192
	v_cvt_pk_f32_fp8_sdwa v[68:69], v192 src0_sel:WORD_1
	v_cvt_pk_f32_fp8_e32 v[70:71], v193
	v_cvt_pk_f32_fp8_sdwa v[72:73], v193 src0_sel:WORD_1
	v_cvt_pk_f32_fp8_e32 v[74:75], v194
	v_cvt_pk_f32_fp8_sdwa v[124:125], v194 src0_sel:WORD_1
	v_pk_fma_f32 v[118:119], v[178:179], v[48:49], v[118:119] op_sel_hi:[1,0,1]
	v_pk_fma_f32 v[122:123], v[180:181], v[48:49], v[122:123] op_sel_hi:[1,0,1]
	v_pk_fma_f32 v[120:121], v[182:183], v[48:49], v[120:121] op_sel_hi:[1,0,1]
	v_pk_fma_f32 v[48:49], v[138:139], v[48:49], v[64:65] op_sel_hi:[1,0,1]
	v_pk_fma_f32 v[118:119], v[184:185], v[50:51], v[118:119] op_sel_hi:[1,0,1]
	v_pk_fma_f32 v[122:123], v[186:187], v[50:51], v[122:123] op_sel_hi:[1,0,1]
	v_pk_fma_f32 v[120:121], v[188:189], v[50:51], v[120:121] op_sel_hi:[1,0,1]
	v_pk_fma_f32 v[48:49], v[140:141], v[50:51], v[48:49] op_sel_hi:[1,0,1]
	v_pk_fma_f32 v[118:119], v[206:207], v[52:53], v[118:119] op_sel_hi:[1,0,1]
	v_pk_fma_f32 v[122:123], v[208:209], v[52:53], v[122:123] op_sel_hi:[1,0,1]
	v_pk_fma_f32 v[120:121], v[210:211], v[52:53], v[120:121] op_sel_hi:[1,0,1]
	v_pk_fma_f32 v[48:49], v[190:191], v[52:53], v[48:49] op_sel_hi:[1,0,1]
	v_cvt_pk_f32_fp8_e32 v[126:127], v195
	v_cvt_pk_f32_fp8_sdwa v[128:129], v195 src0_sel:WORD_1
	v_cvt_pk_f32_fp8_e32 v[130:131], v196
	v_cvt_pk_f32_fp8_sdwa v[132:133], v196 src0_sel:WORD_1
	v_cvt_pk_f32_fp8_e32 v[134:135], v197
	v_cvt_pk_f32_fp8_sdwa v[136:137], v197 src0_sel:WORD_1
	s_waitcnt lgkmcnt(0)
	v_cvt_pk_f32_fp8_e32 v[142:143], v198
	v_cvt_pk_f32_fp8_sdwa v[144:145], v198 src0_sel:WORD_1
	v_cvt_pk_f32_fp8_e32 v[146:147], v199
	v_cvt_pk_f32_fp8_sdwa v[148:149], v199 src0_sel:WORD_1
	v_cvt_pk_f32_fp8_e32 v[150:151], v200
	v_cvt_pk_f32_fp8_sdwa v[152:153], v200 src0_sel:WORD_1
	v_cvt_pk_f32_fp8_e32 v[154:155], v201
	v_cvt_pk_f32_fp8_sdwa v[156:157], v201 src0_sel:WORD_1
	v_cvt_pk_f32_fp8_e32 v[158:159], v202
	v_cvt_pk_f32_fp8_sdwa v[160:161], v202 src0_sel:WORD_1
	v_cvt_pk_f32_fp8_e32 v[162:163], v203
	v_cvt_pk_f32_fp8_sdwa v[164:165], v203 src0_sel:WORD_1
	v_cvt_pk_f32_fp8_e32 v[166:167], v204
	v_cvt_pk_f32_fp8_sdwa v[168:169], v204 src0_sel:WORD_1
	v_cvt_pk_f32_fp8_e32 v[170:171], v205
	v_cvt_pk_f32_fp8_sdwa v[172:173], v205 src0_sel:WORD_1
	s_setprio 0
	s_waitcnt vmcnt(40)
	v_and_b32_e32 v9, 0x1fff8, v46
	v_and_b32_e32 v11, 0x1fff8, v26
	v_and_b32_e32 v13, 0x1fff8, v28
	v_and_b32_e32 v15, 0x1fff8, v30
	ds_read_b64 v[50:51], v9
	ds_read_b64 v[52:53], v11
	ds_read_b64 v[64:65], v13
	ds_read_b64 v[138:139], v15
	v_and_b32_e32 v9, 0x1fff8, v4
	v_and_b32_e32 v11, 0x1fff8, v6
	v_and_b32_e32 v13, 0x1fff8, v8
	v_and_b32_e32 v15, 0x1fff8, v10
	ds_read_b64 v[140:141], v9
	ds_read_b64 v[174:175], v11
	ds_read_b64 v[176:177], v13
	ds_read_b64 v[178:179], v15
	s_setprio 1
	v_pk_fma_f32 v[66:67], v[66:67], v[32:33], v[118:119] op_sel_hi:[1,0,1]
	v_pk_fma_f32 v[68:69], v[68:69], v[32:33], v[122:123] op_sel_hi:[1,0,1]
	v_pk_fma_f32 v[70:71], v[70:71], v[32:33], v[120:121] op_sel_hi:[1,0,1]
	v_pk_fma_f32 v[32:33], v[72:73], v[32:33], v[48:49] op_sel_hi:[1,0,1]
	v_pk_fma_f32 v[66:67], v[74:75], v[34:35], v[66:67] op_sel_hi:[1,0,1]
	v_pk_fma_f32 v[68:69], v[124:125], v[34:35], v[68:69] op_sel_hi:[1,0,1]
	v_pk_fma_f32 v[70:71], v[126:127], v[34:35], v[70:71] op_sel_hi:[1,0,1]
	v_pk_fma_f32 v[32:33], v[128:129], v[34:35], v[32:33] op_sel_hi:[1,0,1]
	v_pk_fma_f32 v[66:67], v[130:131], v[36:37], v[66:67] op_sel_hi:[1,0,1]
	v_pk_fma_f32 v[68:69], v[132:133], v[36:37], v[68:69] op_sel_hi:[1,0,1]
	v_pk_fma_f32 v[70:71], v[134:135], v[36:37], v[70:71] op_sel_hi:[1,0,1]
	v_pk_fma_f32 v[32:33], v[136:137], v[36:37], v[32:33] op_sel_hi:[1,0,1]
	s_waitcnt lgkmcnt(4)
	v_cvt_pk_f32_fp8_e32 v[180:181], v50
	v_cvt_pk_f32_fp8_sdwa v[182:183], v50 src0_sel:WORD_1
	v_cvt_pk_f32_fp8_e32 v[184:185], v51
	v_cvt_pk_f32_fp8_sdwa v[50:51], v51 src0_sel:WORD_1
	v_pk_fma_f32 v[66:67], v[142:143], v[38:39], v[66:67] op_sel_hi:[1,0,1]
	v_pk_fma_f32 v[68:69], v[144:145], v[38:39], v[68:69] op_sel_hi:[1,0,1]
	v_pk_fma_f32 v[70:71], v[146:147], v[38:39], v[70:71] op_sel_hi:[1,0,1]
	v_pk_fma_f32 v[32:33], v[148:149], v[38:39], v[32:33] op_sel_hi:[1,0,1]
	v_cvt_pk_f32_fp8_e32 v[186:187], v52
	v_cvt_pk_f32_fp8_sdwa v[188:189], v52 src0_sel:WORD_1
	v_cvt_pk_f32_fp8_e32 v[190:191], v53
	v_cvt_pk_f32_fp8_sdwa v[52:53], v53 src0_sel:WORD_1
	v_pk_fma_f32 v[66:67], v[150:151], v[40:41], v[66:67] op_sel_hi:[1,0,1]
	v_pk_fma_f32 v[68:69], v[152:153], v[40:41], v[68:69] op_sel_hi:[1,0,1]
	v_pk_fma_f32 v[70:71], v[154:155], v[40:41], v[70:71] op_sel_hi:[1,0,1]
	v_pk_fma_f32 v[32:33], v[156:157], v[40:41], v[32:33] op_sel_hi:[1,0,1]
	v_cvt_pk_f32_fp8_e32 v[192:193], v64
	v_cvt_pk_f32_fp8_sdwa v[194:195], v64 src0_sel:WORD_1
	v_cvt_pk_f32_fp8_e32 v[196:197], v65
	v_cvt_pk_f32_fp8_sdwa v[64:65], v65 src0_sel:WORD_1
	v_pk_fma_f32 v[66:67], v[158:159], v[42:43], v[66:67] op_sel_hi:[1,0,1]
	v_pk_fma_f32 v[68:69], v[160:161], v[42:43], v[68:69] op_sel_hi:[1,0,1]
	v_pk_fma_f32 v[70:71], v[162:163], v[42:43], v[70:71] op_sel_hi:[1,0,1]
	v_pk_fma_f32 v[32:33], v[164:165], v[42:43], v[32:33] op_sel_hi:[1,0,1]
	v_cvt_pk_f32_fp8_e32 v[198:199], v138
	v_cvt_pk_f32_fp8_sdwa v[200:201], v138 src0_sel:WORD_1
	v_cvt_pk_f32_fp8_e32 v[202:203], v139
	v_cvt_pk_f32_fp8_sdwa v[138:139], v139 src0_sel:WORD_1
	v_pk_fma_f32 v[66:67], v[166:167], v[44:45], v[66:67] op_sel_hi:[1,0,1]
	v_pk_fma_f32 v[68:69], v[168:169], v[44:45], v[68:69] op_sel_hi:[1,0,1]
	v_pk_fma_f32 v[70:71], v[170:171], v[44:45], v[70:71] op_sel_hi:[1,0,1]
	v_pk_fma_f32 v[32:33], v[172:173], v[44:45], v[32:33] op_sel_hi:[1,0,1]
	v_pk_fma_f32 v[66:67], v[180:181], v[46:47], v[66:67] op_sel_hi:[1,0,1]
	v_pk_fma_f32 v[68:69], v[182:183], v[46:47], v[68:69] op_sel_hi:[1,0,1]
	v_pk_fma_f32 v[70:71], v[184:185], v[46:47], v[70:71] op_sel_hi:[1,0,1]
	v_pk_fma_f32 v[32:33], v[50:51], v[46:47], v[32:33] op_sel_hi:[1,0,1]
	s_waitcnt lgkmcnt(0)
	v_cvt_pk_f32_fp8_e32 v[34:35], v140
	v_cvt_pk_f32_fp8_sdwa v[36:37], v140 src0_sel:WORD_1
	v_cvt_pk_f32_fp8_e32 v[38:39], v141
	v_cvt_pk_f32_fp8_sdwa v[40:41], v141 src0_sel:WORD_1
	v_cvt_pk_f32_fp8_e32 v[42:43], v174
	v_cvt_pk_f32_fp8_sdwa v[44:45], v174 src0_sel:WORD_1
	v_cvt_pk_f32_fp8_e32 v[46:47], v175
	v_cvt_pk_f32_fp8_sdwa v[48:49], v175 src0_sel:WORD_1
	v_cvt_pk_f32_fp8_e32 v[50:51], v176
	v_cvt_pk_f32_fp8_sdwa v[72:73], v176 src0_sel:WORD_1
	v_cvt_pk_f32_fp8_e32 v[74:75], v177
	v_cvt_pk_f32_fp8_sdwa v[118:119], v177 src0_sel:WORD_1
	v_cvt_pk_f32_fp8_e32 v[120:121], v178
	v_cvt_pk_f32_fp8_sdwa v[122:123], v178 src0_sel:WORD_1
	v_cvt_pk_f32_fp8_e32 v[124:125], v179
	v_pk_fma_f32 v[66:67], v[186:187], v[26:27], v[66:67] op_sel_hi:[1,0,1]
	v_pk_fma_f32 v[68:69], v[188:189], v[26:27], v[68:69] op_sel_hi:[1,0,1]
	v_pk_fma_f32 v[70:71], v[190:191], v[26:27], v[70:71] op_sel_hi:[1,0,1]
	v_pk_fma_f32 v[26:27], v[52:53], v[26:27], v[32:33] op_sel_hi:[1,0,1]
	v_pk_fma_f32 v[66:67], v[192:193], v[28:29], v[66:67] op_sel_hi:[1,0,1]
	v_pk_fma_f32 v[68:69], v[194:195], v[28:29], v[68:69] op_sel_hi:[1,0,1]
	v_pk_fma_f32 v[70:71], v[196:197], v[28:29], v[70:71] op_sel_hi:[1,0,1]
	v_pk_fma_f32 v[26:27], v[64:65], v[28:29], v[26:27] op_sel_hi:[1,0,1]
	v_pk_fma_f32 v[66:67], v[198:199], v[30:31], v[66:67] op_sel_hi:[1,0,1]
	v_pk_fma_f32 v[68:69], v[200:201], v[30:31], v[68:69] op_sel_hi:[1,0,1]
	v_pk_fma_f32 v[70:71], v[202:203], v[30:31], v[70:71] op_sel_hi:[1,0,1]
	v_pk_fma_f32 v[26:27], v[138:139], v[30:31], v[26:27] op_sel_hi:[1,0,1]
	v_cvt_pk_f32_fp8_sdwa v[126:127], v179 src0_sel:WORD_1
	s_setprio 0
	s_waitcnt vmcnt(32)
	v_and_b32_e32 v9, 0x1fff8, v14
	v_and_b32_e32 v11, 0x1fff8, v18
	v_and_b32_e32 v13, 0x1fff8, v20
	v_and_b32_e32 v15, 0x1fff8, v22
	ds_read_b64 v[28:29], v9
	ds_read_b64 v[30:31], v11
	ds_read_b64 v[32:33], v13
	ds_read_b64 v[52:53], v15
	v_and_b32_e32 v9, 0x1fff8, v24
	v_and_b32_e32 v11, 0x1fff8, v12
	v_and_b32_e32 v13, 0x1fff8, v16
	v_and_b32_e32 v15, 0x1fff8, v7
	ds_read_b64 v[64:65], v9
	ds_read_b64 v[128:129], v11
	ds_read_b64 v[130:131], v13
	ds_read_b64 v[132:133], v15
	s_setprio 1
	s_waitcnt lgkmcnt(4)
	v_cvt_pk_f32_fp8_e32 v[134:135], v28
	v_pk_fma_f32 v[34:35], v[34:35], v[4:5], v[66:67] op_sel_hi:[1,0,1]
	v_cvt_pk_f32_fp8_e32 v[140:141], v30
	v_pk_fma_f32 v[34:35], v[42:43], v[6:7], v[34:35] op_sel_hi:[1,0,1]
	v_cvt_pk_f32_fp8_e32 v[146:147], v32
	v_pk_fma_f32 v[34:35], v[50:51], v[8:9], v[34:35] op_sel_hi:[1,0,1]
	v_cvt_pk_f32_fp8_e32 v[152:153], v52
	v_pk_fma_f32 v[34:35], v[120:121], v[10:11], v[34:35] op_sel_hi:[1,0,1]
	s_waitcnt lgkmcnt(0)
	v_cvt_pk_f32_fp8_e32 v[158:159], v64
	v_pk_fma_f32 v[34:35], v[134:135], v[14:15], v[34:35] op_sel_hi:[1,0,1]
	v_cvt_pk_f32_fp8_e32 v[164:165], v128
	v_pk_fma_f32 v[34:35], v[140:141], v[18:19], v[34:35] op_sel_hi:[1,0,1]
	v_cvt_pk_f32_fp8_e32 v[170:171], v130
	v_pk_fma_f32 v[34:35], v[146:147], v[20:21], v[34:35] op_sel_hi:[1,0,1]
	v_cvt_pk_f32_fp8_sdwa v[136:137], v28 src0_sel:WORD_1
	v_pk_fma_f32 v[34:35], v[152:153], v[22:23], v[34:35] op_sel_hi:[1,0,1]
	v_cvt_pk_f32_fp8_sdwa v[142:143], v30 src0_sel:WORD_1
	v_pk_fma_f32 v[34:35], v[158:159], v[24:25], v[34:35] op_sel_hi:[1,0,1]
	v_cvt_pk_f32_fp8_sdwa v[148:149], v32 src0_sel:WORD_1
	v_pk_fma_f32 v[34:35], v[164:165], v[12:13], v[34:35] op_sel_hi:[1,0,1]
	v_cvt_pk_f32_fp8_sdwa v[154:155], v52 src0_sel:WORD_1
	v_pk_fma_f32 v[120:121], v[170:171], v[16:17], v[34:35] op_sel_hi:[1,0,1]
	v_pk_fma_f32 v[34:35], v[36:37], v[4:5], v[68:69] op_sel_hi:[1,0,1]
	v_cvt_pk_f32_fp8_sdwa v[160:161], v64 src0_sel:WORD_1
	v_pk_fma_f32 v[34:35], v[44:45], v[6:7], v[34:35] op_sel_hi:[1,0,1]
	v_cvt_pk_f32_fp8_sdwa v[166:167], v128 src0_sel:WORD_1
	v_pk_fma_f32 v[34:35], v[72:73], v[8:9], v[34:35] op_sel_hi:[1,0,1]
	v_cvt_pk_f32_fp8_sdwa v[172:173], v130 src0_sel:WORD_1
	v_pk_fma_f32 v[34:35], v[122:123], v[10:11], v[34:35] op_sel_hi:[1,0,1]
	v_cvt_pk_f32_fp8_e32 v[138:139], v29
	v_pk_fma_f32 v[34:35], v[136:137], v[14:15], v[34:35] op_sel_hi:[1,0,1]
	v_cvt_pk_f32_fp8_sdwa v[28:29], v29 src0_sel:WORD_1
	v_pk_fma_f32 v[34:35], v[142:143], v[18:19], v[34:35] op_sel_hi:[1,0,1]
	v_cvt_pk_f32_fp8_e32 v[144:145], v31
	v_pk_fma_f32 v[34:35], v[148:149], v[20:21], v[34:35] op_sel_hi:[1,0,1]
	v_pk_fma_f32 v[26:27], v[40:41], v[4:5], v[26:27] op_sel_hi:[1,0,1]
	v_pk_fma_f32 v[34:35], v[154:155], v[22:23], v[34:35] op_sel_hi:[1,0,1]
	v_cvt_pk_f32_fp8_sdwa v[30:31], v31 src0_sel:WORD_1
	v_pk_fma_f32 v[34:35], v[160:161], v[24:25], v[34:35] op_sel_hi:[1,0,1]
	v_cvt_pk_f32_fp8_e32 v[150:151], v33
	v_pk_fma_f32 v[34:35], v[166:167], v[12:13], v[34:35] op_sel_hi:[1,0,1]
	v_pk_fma_f32 v[26:27], v[48:49], v[6:7], v[26:27] op_sel_hi:[1,0,1]
	v_pk_fma_f32 v[122:123], v[172:173], v[16:17], v[34:35] op_sel_hi:[1,0,1]
	v_pk_fma_f32 v[34:35], v[38:39], v[4:5], v[70:71] op_sel_hi:[1,0,1]
	v_cvt_pk_f32_fp8_sdwa v[32:33], v33 src0_sel:WORD_1
	v_pk_fma_f32 v[34:35], v[46:47], v[6:7], v[34:35] op_sel_hi:[1,0,1]
	v_cvt_pk_f32_fp8_e32 v[156:157], v53
	v_pk_fma_f32 v[34:35], v[74:75], v[8:9], v[34:35] op_sel_hi:[1,0,1]
	v_pk_fma_f32 v[8:9], v[118:119], v[8:9], v[26:27] op_sel_hi:[1,0,1]
	v_pk_fma_f32 v[34:35], v[124:125], v[10:11], v[34:35] op_sel_hi:[1,0,1]
	v_cvt_pk_f32_fp8_sdwa v[52:53], v53 src0_sel:WORD_1
	v_cvt_pk_f32_fp8_e32 v[162:163], v65
	v_pk_fma_f32 v[34:35], v[138:139], v[14:15], v[34:35] op_sel_hi:[1,0,1]
	v_pk_fma_f32 v[8:9], v[126:127], v[10:11], v[8:9] op_sel_hi:[1,0,1]
	v_cvt_pk_f32_fp8_sdwa v[64:65], v65 src0_sel:WORD_1
	v_cvt_pk_f32_fp8_e32 v[168:169], v129
	v_pk_fma_f32 v[34:35], v[144:145], v[18:19], v[34:35] op_sel_hi:[1,0,1]
; template <int VVAR> __device__ __forceinline__ void peer_v_phase(LAS unsigned char* lds, int wave, int vcu, const unsigned char* __restrict__ VS_l, const unsigned* __restrict__ PW, bf16* __restrict__ Y) {
;     ...
; #pragma unroll 1
;     for (int it = 0; it < (VVAR == 5 ? 2 : 64); it += 2) {
;         V_HALF(pa, pb, it + 1);
;         V_HALF(pb, pa, it + 2);
	v_pk_fma_f32 v[8:9], v[28:29], v[14:15], v[8:9] op_sel_hi:[1,0,1]
	v_cvt_pk_f32_fp8_sdwa v[128:129], v129 src0_sel:WORD_1
	v_cvt_pk_f32_fp8_e32 v[174:175], v131
	v_pk_fma_f32 v[34:35], v[150:151], v[20:21], v[34:35] op_sel_hi:[1,0,1]
	v_pk_fma_f32 v[8:9], v[30:31], v[18:19], v[8:9] op_sel_hi:[1,0,1]
	v_cvt_pk_f32_fp8_sdwa v[130:131], v131 src0_sel:WORD_1
	v_pk_fma_f32 v[34:35], v[156:157], v[22:23], v[34:35] op_sel_hi:[1,0,1]
	v_pk_fma_f32 v[8:9], v[32:33], v[20:21], v[8:9] op_sel_hi:[1,0,1]
	v_cvt_pk_f32_fp8_e32 v[118:119], v132
	v_pk_fma_f32 v[34:35], v[162:163], v[24:25], v[34:35] op_sel_hi:[1,0,1]
	v_pk_fma_f32 v[8:9], v[52:53], v[22:23], v[8:9] op_sel_hi:[1,0,1]
	v_pk_fma_f32 v[34:35], v[168:169], v[12:13], v[34:35] op_sel_hi:[1,0,1]
	v_pk_fma_f32 v[8:9], v[64:65], v[24:25], v[8:9] op_sel_hi:[1,0,1]
	v_pk_fma_f32 v[124:125], v[174:175], v[16:17], v[34:35] op_sel_hi:[1,0,1]
	v_pk_fma_f32 v[8:9], v[128:129], v[12:13], v[8:9] op_sel_hi:[1,0,1]
	v_cvt_pk_f32_fp8_sdwa v[126:127], v132 src0_sel:WORD_1
	v_cvt_pk_f32_fp8_e32 v[134:135], v133
	v_cvt_pk_f32_fp8_sdwa v[132:133], v133 src0_sel:WORD_1
	v_pk_fma_f32 v[128:129], v[130:131], v[16:17], v[8:9] op_sel_hi:[1,0,1]
	v_mov_b32_e32 v130, v7
	s_setprio 0
	s_add_i32 s18, s18, 2
	s_cmp_gt_u32 s17, 61
	s_cselect_b64 s[10:11], -1, 0
	s_cmp_lt_u32 s17, 62
	s_cselect_b32 s19, s18, 63
	s_lshl_b32 s20, s19, 1
	s_and_b32 s20, s20, 0xf8
	s_add_i32 s20, s20, s4
	s_ashr_i32 s21, s20, 31
	s_lshl_b64 s[20:21], s[20:21], 15
	s_add_u32 s20, s12, s20
	s_addc_u32 s21, s13, s21
	s_lshl_b32 s19, s19, 13
	s_and_b32 s19, s19, 0x6000
	s_add_u32 s20, s20, s19
	s_addc_u32 s21, s21, 0
	s_add_u32 s66, s20, s5
	s_addc_u32 s67, s21, 0
	global_load_dword v64, v2, s[20:21]
	global_load_dword v66, v2, s[20:21] offset:256
	global_load_dword v68, v2, s[20:21] offset:512
	global_load_dword v70, v2, s[20:21] offset:768
	global_load_dword v72, v2, s[20:21] offset:1024
	global_load_dword v74, v2, s[20:21] offset:1280
	global_load_dword v48, v2, s[20:21] offset:1536
	global_load_dword v50, v2, s[20:21] offset:1792
	global_load_dword v52, v2, s[20:21] offset:2048
	global_load_dword v32, v2, s[20:21] offset:2304
	global_load_dword v34, v2, s[20:21] offset:2560
	global_load_dword v36, v2, s[20:21] offset:2816
	global_load_dword v38, v2, s[20:21] offset:3072
	global_load_dword v40, v2, s[20:21] offset:3328
	global_load_dword v42, v2, s[20:21] offset:3584
	global_load_dword v44, v2, s[20:21] offset:3840
	global_load_dword v46, v2, s[66:67]
	global_load_dword v26, v2, s[66:67] offset:256
	global_load_dword v28, v2, s[66:67] offset:512
	global_load_dword v30, v2, s[66:67] offset:768
	global_load_dword v4, v2, s[66:67] offset:1024
	global_load_dword v6, v2, s[66:67] offset:1280
	global_load_dword v8, v2, s[66:67] offset:1536
	global_load_dword v10, v2, s[66:67] offset:1792
	global_load_dword v14, v2, s[66:67] offset:2048
	global_load_dword v18, v2, s[66:67] offset:2304
	global_load_dword v20, v2, s[66:67] offset:2560
	global_load_dword v22, v2, s[66:67] offset:2816
	global_load_dword v24, v2, s[66:67] offset:3072
	global_load_dword v12, v2, s[66:67] offset:3328
	global_load_dword v16, v2, s[66:67] offset:3584
	global_load_dword v7, v2, s[66:67] offset:3840
	s_waitcnt vmcnt(55)
	v_and_b32_e32 v9, 0x1fff8, v116
	v_and_b32_e32 v11, 0x1fff8, v104
	v_and_b32_e32 v13, 0x1fff8, v106
	v_and_b32_e32 v15, 0x1fff8, v108
	ds_read_b64 v[136:137], v9
	ds_read_b64 v[138:139], v11
	ds_read_b64 v[140:141], v13
	ds_read_b64 v[142:143], v15
	v_and_b32_e32 v9, 0x1fff8, v110
	v_and_b32_e32 v11, 0x1fff8, v112
	v_and_b32_e32 v13, 0x1fff8, v114
	v_and_b32_e32 v15, 0x1fff8, v98
	ds_read_b64 v[144:145], v9
	ds_read_b64 v[146:147], v11
	ds_read_b64 v[148:149], v13
	ds_read_b64 v[150:151], v15
	s_setprio 1
	s_waitcnt lgkmcnt(4)
	v_cvt_pk_f32_fp8_e32 v[152:153], v136
	v_cvt_pk_f32_fp8_sdwa v[154:155], v136 src0_sel:WORD_1
	v_cvt_pk_f32_fp8_e32 v[156:157], v137
	v_cvt_pk_f32_fp8_sdwa v[136:137], v137 src0_sel:WORD_1
	v_cvt_pk_f32_fp8_e32 v[158:159], v138
	v_cvt_pk_f32_fp8_sdwa v[160:161], v138 src0_sel:WORD_1
	v_cvt_pk_f32_fp8_e32 v[162:163], v139
	v_cvt_pk_f32_fp8_sdwa v[138:139], v139 src0_sel:WORD_1
	v_cvt_pk_f32_fp8_e32 v[164:165], v140
	v_cvt_pk_f32_fp8_sdwa v[166:167], v140 src0_sel:WORD_1
	v_cvt_pk_f32_fp8_e32 v[168:169], v141
	v_cvt_pk_f32_fp8_sdwa v[140:141], v141 src0_sel:WORD_1
	v_cvt_pk_f32_fp8_e32 v[170:171], v142
	v_cvt_pk_f32_fp8_sdwa v[172:173], v142 src0_sel:WORD_1
	v_cvt_pk_f32_fp8_e32 v[174:175], v143
	v_cvt_pk_f32_fp8_sdwa v[142:143], v143 src0_sel:WORD_1
	s_waitcnt lgkmcnt(0)
	v_cvt_pk_f32_fp8_e32 v[176:177], v144
	v_cvt_pk_f32_fp8_sdwa v[178:179], v144 src0_sel:WORD_1
	v_cvt_pk_f32_fp8_e32 v[180:181], v145
	v_cvt_pk_f32_fp8_sdwa v[144:145], v145 src0_sel:WORD_1
	v_cvt_pk_f32_fp8_e32 v[182:183], v146
	v_cvt_pk_f32_fp8_sdwa v[184:185], v146 src0_sel:WORD_1
	v_cvt_pk_f32_fp8_e32 v[186:187], v147
	v_cvt_pk_f32_fp8_sdwa v[146:147], v147 src0_sel:WORD_1
	v_cvt_pk_f32_fp8_e32 v[188:189], v148
	v_cvt_pk_f32_fp8_sdwa v[190:191], v148 src0_sel:WORD_1
	v_cvt_pk_f32_fp8_e32 v[192:193], v149
	v_cvt_pk_f32_fp8_sdwa v[148:149], v149 src0_sel:WORD_1
	v_cvt_pk_f32_fp8_e32 v[194:195], v150
	v_cvt_pk_f32_fp8_sdwa v[196:197], v150 src0_sel:WORD_1
	v_cvt_pk_f32_fp8_e32 v[198:199], v151
	v_cvt_pk_f32_fp8_sdwa v[150:151], v151 src0_sel:WORD_1
	s_setprio 0
	v_and_b32_e32 v9, 0x1fff8, v100
	s_waitcnt vmcnt(48)
	v_and_b32_e32 v11, 0x1fff8, v102
	v_and_b32_e32 v13, 0x1fff8, v78
	v_and_b32_e32 v15, 0x1fff8, v80
	ds_read_b64 v[200:201], v9
	ds_read_b64 v[202:203], v11
	ds_read_b64 v[204:205], v13
	ds_read_b64 v[206:207], v15
	v_and_b32_e32 v9, 0x1fff8, v82
	v_and_b32_e32 v11, 0x1fff8, v84
	v_and_b32_e32 v13, 0x1fff8, v86
	v_and_b32_e32 v15, 0x1fff8, v88
	ds_read_b64 v[208:209], v9
	ds_read_b64 v[210:211], v11
	ds_read_b64 v[212:213], v13
	ds_read_b64 v[214:215], v15
	s_setprio 1
	v_pk_fma_f32 v[118:119], v[118:119], v[130:131], v[120:121] op_sel_hi:[1,0,1]
	v_pk_fma_f32 v[120:121], v[126:127], v[130:131], v[122:123] op_sel_hi:[1,0,1]
	v_pk_fma_f32 v[122:123], v[134:135], v[130:131], v[124:125] op_sel_hi:[1,0,1]
	v_pk_fma_f32 v[118:119], v[152:153], v[116:117], v[118:119] op_sel_hi:[1,0,1]
	v_pk_fma_f32 v[120:121], v[154:155], v[116:117], v[120:121] op_sel_hi:[1,0,1]
	v_pk_fma_f32 v[122:123], v[156:157], v[116:117], v[122:123] op_sel_hi:[1,0,1]
	v_pk_fma_f32 v[124:125], v[132:133], v[130:131], v[128:129] op_sel_hi:[1,0,1]
	v_pk_fma_f32 v[118:119], v[158:159], v[104:105], v[118:119] op_sel_hi:[1,0,1]
	v_pk_fma_f32 v[120:121], v[160:161], v[104:105], v[120:121] op_sel_hi:[1,0,1]
	v_pk_fma_f32 v[122:123], v[162:163], v[104:105], v[122:123] op_sel_hi:[1,0,1]
	v_pk_fma_f32 v[116:117], v[136:137], v[116:117], v[124:125] op_sel_hi:[1,0,1]
	v_pk_fma_f32 v[118:119], v[164:165], v[106:107], v[118:119] op_sel_hi:[1,0,1]
	v_pk_fma_f32 v[120:121], v[166:167], v[106:107], v[120:121] op_sel_hi:[1,0,1]
	v_pk_fma_f32 v[122:123], v[168:169], v[106:107], v[122:123] op_sel_hi:[1,0,1]
	v_pk_fma_f32 v[104:105], v[138:139], v[104:105], v[116:117] op_sel_hi:[1,0,1]
	v_pk_fma_f32 v[118:119], v[170:171], v[108:109], v[118:119] op_sel_hi:[1,0,1]
	v_pk_fma_f32 v[120:121], v[172:173], v[108:109], v[120:121] op_sel_hi:[1,0,1]
	v_pk_fma_f32 v[122:123], v[174:175], v[108:109], v[122:123] op_sel_hi:[1,0,1]
	v_pk_fma_f32 v[104:105], v[140:141], v[106:107], v[104:105] op_sel_hi:[1,0,1]
	s_waitcnt lgkmcnt(4)
	v_cvt_pk_f32_fp8_e32 v[216:217], v200
	v_cvt_pk_f32_fp8_sdwa v[218:219], v200 src0_sel:WORD_1
	v_cvt_pk_f32_fp8_e32 v[220:221], v201
	v_pk_fma_f32 v[118:119], v[176:177], v[110:111], v[118:119] op_sel_hi:[1,0,1]
	v_pk_fma_f32 v[120:121], v[178:179], v[110:111], v[120:121] op_sel_hi:[1,0,1]
	v_pk_fma_f32 v[122:123], v[180:181], v[110:111], v[122:123] op_sel_hi:[1,0,1]
	v_pk_fma_f32 v[104:105], v[142:143], v[108:109], v[104:105] op_sel_hi:[1,0,1]
	v_cvt_pk_f32_fp8_sdwa v[200:201], v201 src0_sel:WORD_1
	v_cvt_pk_f32_fp8_e32 v[222:223], v202
	v_cvt_pk_f32_fp8_sdwa v[224:225], v202 src0_sel:WORD_1
	v_cvt_pk_f32_fp8_e32 v[226:227], v203
	v_pk_fma_f32 v[118:119], v[182:183], v[112:113], v[118:119] op_sel_hi:[1,0,1]
	v_pk_fma_f32 v[120:121], v[184:185], v[112:113], v[120:121] op_sel_hi:[1,0,1]
	v_pk_fma_f32 v[122:123], v[186:187], v[112:113], v[122:123] op_sel_hi:[1,0,1]
	v_pk_fma_f32 v[104:105], v[144:145], v[110:111], v[104:105] op_sel_hi:[1,0,1]
	v_cvt_pk_f32_fp8_sdwa v[202:203], v203 src0_sel:WORD_1
	v_pk_fma_f32 v[118:119], v[188:189], v[114:115], v[118:119] op_sel_hi:[1,0,1]
	v_pk_fma_f32 v[120:121], v[190:191], v[114:115], v[120:121] op_sel_hi:[1,0,1]
	v_pk_fma_f32 v[122:123], v[192:193], v[114:115], v[122:123] op_sel_hi:[1,0,1]
	v_pk_fma_f32 v[104:105], v[146:147], v[112:113], v[104:105] op_sel_hi:[1,0,1]
	v_cvt_pk_f32_fp8_e32 v[124:125], v207
	v_pk_fma_f32 v[118:119], v[194:195], v[98:99], v[118:119] op_sel_hi:[1,0,1]
	v_pk_fma_f32 v[120:121], v[196:197], v[98:99], v[120:121] op_sel_hi:[1,0,1]
	v_pk_fma_f32 v[122:123], v[198:199], v[98:99], v[122:123] op_sel_hi:[1,0,1]
	v_pk_fma_f32 v[104:105], v[148:149], v[114:115], v[104:105] op_sel_hi:[1,0,1]
	v_pk_fma_f32 v[118:119], v[216:217], v[100:101], v[118:119] op_sel_hi:[1,0,1]
	v_pk_fma_f32 v[120:121], v[218:219], v[100:101], v[120:121] op_sel_hi:[1,0,1]
	v_pk_fma_f32 v[122:123], v[220:221], v[100:101], v[122:123] op_sel_hi:[1,0,1]
	v_pk_fma_f32 v[98:99], v[150:151], v[98:99], v[104:105] op_sel_hi:[1,0,1]
	v_pk_fma_f32 v[118:119], v[222:223], v[102:103], v[118:119] op_sel_hi:[1,0,1]
	v_pk_fma_f32 v[120:121], v[224:225], v[102:103], v[120:121] op_sel_hi:[1,0,1]
	v_pk_fma_f32 v[122:123], v[226:227], v[102:103], v[122:123] op_sel_hi:[1,0,1]
	v_pk_fma_f32 v[98:99], v[200:201], v[100:101], v[98:99] op_sel_hi:[1,0,1]
	v_cvt_pk_f32_fp8_e32 v[106:107], v204
	v_cvt_pk_f32_fp8_sdwa v[108:109], v204 src0_sel:WORD_1
	v_cvt_pk_f32_fp8_e32 v[110:111], v205
	v_cvt_pk_f32_fp8_sdwa v[112:113], v205 src0_sel:WORD_1
	v_cvt_pk_f32_fp8_e32 v[114:115], v206
	v_cvt_pk_f32_fp8_sdwa v[116:117], v206 src0_sel:WORD_1
	v_cvt_pk_f32_fp8_sdwa v[126:127], v207 src0_sel:WORD_1
	s_waitcnt lgkmcnt(0)
	v_cvt_pk_f32_fp8_e32 v[128:129], v208
	v_cvt_pk_f32_fp8_sdwa v[130:131], v208 src0_sel:WORD_1
	v_cvt_pk_f32_fp8_e32 v[132:133], v209
	v_cvt_pk_f32_fp8_sdwa v[134:135], v209 src0_sel:WORD_1
	v_cvt_pk_f32_fp8_e32 v[136:137], v210
	v_cvt_pk_f32_fp8_sdwa v[138:139], v210 src0_sel:WORD_1
	v_cvt_pk_f32_fp8_e32 v[140:141], v211
	v_cvt_pk_f32_fp8_sdwa v[142:143], v211 src0_sel:WORD_1
	v_cvt_pk_f32_fp8_e32 v[144:145], v212
	v_cvt_pk_f32_fp8_sdwa v[146:147], v212 src0_sel:WORD_1
	v_cvt_pk_f32_fp8_e32 v[148:149], v213
	v_cvt_pk_f32_fp8_sdwa v[152:153], v213 src0_sel:WORD_1
	v_cvt_pk_f32_fp8_e32 v[154:155], v214
	v_cvt_pk_f32_fp8_sdwa v[156:157], v214 src0_sel:WORD_1
	v_cvt_pk_f32_fp8_e32 v[158:159], v215
	v_cvt_pk_f32_fp8_sdwa v[160:161], v215 src0_sel:WORD_1
	v_pk_fma_f32 v[98:99], v[202:203], v[102:103], v[98:99] op_sel_hi:[1,0,1]
	s_setprio 0
	s_waitcnt vmcnt(40)
	v_and_b32_e32 v9, 0x1fff8, v90
	v_and_b32_e32 v11, 0x1fff8, v92
	v_and_b32_e32 v13, 0x1fff8, v94
	v_and_b32_e32 v15, 0x1fff8, v96
	ds_read_b64 v[100:101], v9
	ds_read_b64 v[102:103], v11
	ds_read_b64 v[104:105], v13
	ds_read_b64 v[150:151], v15
	v_and_b32_e32 v9, 0x1fff8, v76
	v_and_b32_e32 v11, 0x1fff8, v77
	v_and_b32_e32 v13, 0x1fff8, v56
	v_and_b32_e32 v15, 0x1fff8, v57
	ds_read_b64 v[162:163], v9
	ds_read_b64 v[164:165], v11
	ds_read_b64 v[166:167], v13
	ds_read_b64 v[168:169], v15
	s_setprio 1
	v_pk_fma_f32 v[106:107], v[106:107], v[78:79], v[118:119] op_sel_hi:[1,0,1]
	v_pk_fma_f32 v[108:109], v[108:109], v[78:79], v[120:121] op_sel_hi:[1,0,1]
	v_pk_fma_f32 v[110:111], v[110:111], v[78:79], v[122:123] op_sel_hi:[1,0,1]
	v_pk_fma_f32 v[78:79], v[112:113], v[78:79], v[98:99] op_sel_hi:[1,0,1]
	v_pk_fma_f32 v[106:107], v[114:115], v[80:81], v[106:107] op_sel_hi:[1,0,1]
	v_pk_fma_f32 v[108:109], v[116:117], v[80:81], v[108:109] op_sel_hi:[1,0,1]
	v_pk_fma_f32 v[110:111], v[124:125], v[80:81], v[110:111] op_sel_hi:[1,0,1]
	v_pk_fma_f32 v[78:79], v[126:127], v[80:81], v[78:79] op_sel_hi:[1,0,1]
	s_waitcnt lgkmcnt(4)
	v_cvt_pk_f32_fp8_e32 v[170:171], v100
	v_cvt_pk_f32_fp8_sdwa v[172:173], v100 src0_sel:WORD_1
	v_cvt_pk_f32_fp8_e32 v[174:175], v101
	v_cvt_pk_f32_fp8_sdwa v[100:101], v101 src0_sel:WORD_1
	v_pk_fma_f32 v[106:107], v[128:129], v[82:83], v[106:107] op_sel_hi:[1,0,1]
	v_pk_fma_f32 v[108:109], v[130:131], v[82:83], v[108:109] op_sel_hi:[1,0,1]
	v_pk_fma_f32 v[110:111], v[132:133], v[82:83], v[110:111] op_sel_hi:[1,0,1]
	v_pk_fma_f32 v[78:79], v[134:135], v[82:83], v[78:79] op_sel_hi:[1,0,1]
	v_cvt_pk_f32_fp8_e32 v[176:177], v102
	v_cvt_pk_f32_fp8_sdwa v[178:179], v102 src0_sel:WORD_1
	v_cvt_pk_f32_fp8_e32 v[180:181], v103
	v_cvt_pk_f32_fp8_sdwa v[102:103], v103 src0_sel:WORD_1
	v_pk_fma_f32 v[106:107], v[136:137], v[84:85], v[106:107] op_sel_hi:[1,0,1]
	v_pk_fma_f32 v[108:109], v[138:139], v[84:85], v[108:109] op_sel_hi:[1,0,1]
	v_pk_fma_f32 v[110:111], v[140:141], v[84:85], v[110:111] op_sel_hi:[1,0,1]
	v_pk_fma_f32 v[78:79], v[142:143], v[84:85], v[78:79] op_sel_hi:[1,0,1]
	v_cvt_pk_f32_fp8_e32 v[182:183], v104
	v_cvt_pk_f32_fp8_sdwa v[184:185], v104 src0_sel:WORD_1
	v_cvt_pk_f32_fp8_e32 v[186:187], v105
	v_cvt_pk_f32_fp8_sdwa v[104:105], v105 src0_sel:WORD_1
	v_pk_fma_f32 v[106:107], v[144:145], v[86:87], v[106:107] op_sel_hi:[1,0,1]
	v_pk_fma_f32 v[108:109], v[146:147], v[86:87], v[108:109] op_sel_hi:[1,0,1]
	v_pk_fma_f32 v[110:111], v[148:149], v[86:87], v[110:111] op_sel_hi:[1,0,1]
	v_pk_fma_f32 v[78:79], v[152:153], v[86:87], v[78:79] op_sel_hi:[1,0,1]
	v_pk_fma_f32 v[106:107], v[154:155], v[88:89], v[106:107] op_sel_hi:[1,0,1]
	v_pk_fma_f32 v[108:109], v[156:157], v[88:89], v[108:109] op_sel_hi:[1,0,1]
	v_pk_fma_f32 v[110:111], v[158:159], v[88:89], v[110:111] op_sel_hi:[1,0,1]
	v_pk_fma_f32 v[78:79], v[160:161], v[88:89], v[78:79] op_sel_hi:[1,0,1]
	s_waitcnt lgkmcnt(0)
	v_cvt_pk_f32_fp8_e32 v[194:195], v162
	v_cvt_pk_f32_fp8_sdwa v[196:197], v162 src0_sel:WORD_1
	v_cvt_pk_f32_fp8_e32 v[198:199], v163
	v_cvt_pk_f32_fp8_sdwa v[162:163], v163 src0_sel:WORD_1
	v_cvt_pk_f32_fp8_e32 v[200:201], v164
	v_cvt_pk_f32_fp8_sdwa v[202:203], v164 src0_sel:WORD_1
	v_cvt_pk_f32_fp8_e32 v[204:205], v165
	v_cvt_pk_f32_fp8_sdwa v[164:165], v165 src0_sel:WORD_1
	v_pk_fma_f32 v[106:107], v[170:171], v[90:91], v[106:107] op_sel_hi:[1,0,1]
	v_pk_fma_f32 v[108:109], v[172:173], v[90:91], v[108:109] op_sel_hi:[1,0,1]
	v_pk_fma_f32 v[110:111], v[174:175], v[90:91], v[110:111] op_sel_hi:[1,0,1]
	v_pk_fma_f32 v[78:79], v[100:101], v[90:91], v[78:79] op_sel_hi:[1,0,1]
	v_pk_fma_f32 v[106:107], v[176:177], v[92:93], v[106:107] op_sel_hi:[1,0,1]
	v_pk_fma_f32 v[108:109], v[178:179], v[92:93], v[108:109] op_sel_hi:[1,0,1]
	v_pk_fma_f32 v[110:111], v[180:181], v[92:93], v[110:111] op_sel_hi:[1,0,1]
	v_pk_fma_f32 v[78:79], v[102:103], v[92:93], v[78:79] op_sel_hi:[1,0,1]
	v_cvt_pk_f32_fp8_e32 v[188:189], v150
	v_cvt_pk_f32_fp8_sdwa v[190:191], v150 src0_sel:WORD_1
	v_cvt_pk_f32_fp8_e32 v[192:193], v151
	v_cvt_pk_f32_fp8_sdwa v[150:151], v151 src0_sel:WORD_1
	v_pk_fma_f32 v[106:107], v[182:183], v[94:95], v[106:107] op_sel_hi:[1,0,1]
	v_pk_fma_f32 v[108:109], v[184:185], v[94:95], v[108:109] op_sel_hi:[1,0,1]
	v_pk_fma_f32 v[110:111], v[186:187], v[94:95], v[110:111] op_sel_hi:[1,0,1]
	v_pk_fma_f32 v[78:79], v[104:105], v[94:95], v[78:79] op_sel_hi:[1,0,1]
	v_cvt_pk_f32_fp8_sdwa v[88:89], v167 src0_sel:WORD_1
	v_cvt_pk_f32_fp8_sdwa v[94:95], v169 src0_sel:WORD_1
	v_pk_fma_f32 v[78:79], v[162:163], v[76:77], v[78:79] op_sel_hi:[1,0,1]
	v_pk_fma_f32 v[106:107], v[188:189], v[96:97], v[106:107] op_sel_hi:[1,0,1]
	v_pk_fma_f32 v[108:109], v[190:191], v[96:97], v[108:109] op_sel_hi:[1,0,1]
	v_pk_fma_f32 v[110:111], v[192:193], v[96:97], v[110:111] op_sel_hi:[1,0,1]
	v_pk_fma_f32 v[78:79], v[150:151], v[96:97], v[78:79] op_sel_hi:[1,0,1]
	v_pk_fma_f32 v[78:79], v[88:89], v[56:57], v[78:79] op_sel_hi:[1,0,1]
	v_pk_fma_f32 v[106:107], v[194:195], v[76:77], v[106:107] op_sel_hi:[1,0,1]
	v_pk_fma_f32 v[108:109], v[196:197], v[76:77], v[108:109] op_sel_hi:[1,0,1]
	v_pk_fma_f32 v[110:111], v[198:199], v[76:77], v[110:111] op_sel_hi:[1,0,1]
	v_pk_fma_f32 v[78:79], v[164:165], v[76:77], v[78:79] op_sel:[0,1,0] op_sel_hi:[1,1,1]
	v_cvt_pk_f32_fp8_e32 v[82:83], v166
	v_cvt_pk_f32_fp8_sdwa v[84:85], v166 src0_sel:WORD_1
	v_cvt_pk_f32_fp8_e32 v[86:87], v167
	v_cvt_pk_f32_fp8_e32 v[90:91], v168
	v_cvt_pk_f32_fp8_sdwa v[92:93], v168 src0_sel:WORD_1
	v_cvt_pk_f32_fp8_e32 v[96:97], v169
	v_pk_fma_f32 v[78:79], v[94:95], v[56:57], v[78:79] op_sel:[0,1,0] op_sel_hi:[1,1,1]
	s_setprio 0
	s_waitcnt vmcnt(32)
; #define GAS __attribute__((address_space(1)))
; __device__ __forceinline__ unsigned f2bf(float f) { unsigned u = __builtin_bit_cast(unsigned, f); return (u + 0x7fffu + ((u >> 16) & 1u)) >> 16; }
; template <int VVAR> __device__ __forceinline__ void peer_v_phase(LAS unsigned char* lds, int wave, int vcu, const unsigned char* __restrict__ VS_l, const unsigned* __restrict__ PW, bf16* __restrict__ Y) {
;     ...
; #pragma unroll 1
;     for (int it = 0; it < (VVAR == 5 ? 2 : 64); it += 2) {
;         V_HALF(pa, pb, it + 1);
;         V_HALF(pb, pa, it + 2);
;         if ((it & 3) == 2) {
;             const int blk = th * 128 + wave + 8 * (it >> 2);
;             bf16* yp = Y + ((size_t)blk * 1024 + cs * 8) * 64 + lane;
; #pragma unroll
;             for (int c = 0; c < 8; ++c) ((GAS unsigned short*)yp)[c * 64] = (unsigned short)f2bf(acc[c]);
; #pragma unroll
;             for (int c = 0; c < 8; ++c) acc[c] = 0.f;
;         }
	v_and_b32_e32 v9, 0x1fff8, v58
	v_and_b32_e32 v11, 0x1fff8, v59
	v_and_b32_e32 v13, 0x1fff8, v60
	v_and_b32_e32 v15, 0x1fff8, v61
	ds_read_b64 v[100:101], v9
	ds_read_b64 v[102:103], v11
	ds_read_b64 v[104:105], v13
	ds_read_b64 v[112:113], v15
	v_and_b32_e32 v9, 0x1fff8, v62
	v_and_b32_e32 v11, 0x1fff8, v63
	v_and_b32_e32 v13, 0x1fff8, v54
	v_and_b32_e32 v15, 0x1fff8, v55
	ds_read_b64 v[114:115], v9
	ds_read_b64 v[118:119], v11
	ds_read_b64 v[120:121], v13
	ds_read_b64 v[122:123], v15
	s_setprio 1
	s_waitcnt lgkmcnt(4)
	v_cvt_pk_f32_fp8_e32 v[124:125], v100
	v_cvt_pk_f32_fp8_sdwa v[126:127], v100 src0_sel:WORD_1
	v_cvt_pk_f32_fp8_e32 v[128:129], v101
	v_cvt_pk_f32_fp8_sdwa v[100:101], v101 src0_sel:WORD_1
	v_cvt_pk_f32_fp8_sdwa v[134:135], v103 src0_sel:WORD_1
	v_cvt_pk_f32_fp8_e32 v[130:131], v102
	v_cvt_pk_f32_fp8_e32 v[138:139], v104
	v_cvt_pk_f32_fp8_sdwa v[140:141], v104 src0_sel:WORD_1
	v_cvt_pk_f32_fp8_e32 v[142:143], v105
	v_cvt_pk_f32_fp8_sdwa v[104:105], v105 src0_sel:WORD_1
	v_cvt_pk_f32_fp8_sdwa v[148:149], v113 src0_sel:WORD_1
	v_pk_fma_f32 v[106:107], v[200:201], v[76:77], v[106:107] op_sel:[0,1,0] op_sel_hi:[1,1,1]
	s_waitcnt lgkmcnt(0)
	v_cvt_pk_f32_fp8_e32 v[152:153], v114
	v_cvt_pk_f32_fp8_sdwa v[154:155], v114 src0_sel:WORD_1
	v_cvt_pk_f32_fp8_e32 v[156:157], v115
	v_cvt_pk_f32_fp8_sdwa v[114:115], v115 src0_sel:WORD_1
	v_cvt_pk_f32_fp8_sdwa v[162:163], v119 src0_sel:WORD_1
	v_pk_fma_f32 v[82:83], v[82:83], v[56:57], v[106:107] op_sel_hi:[1,0,1]
	v_cvt_pk_f32_fp8_e32 v[144:145], v112
	v_cvt_pk_f32_fp8_e32 v[158:159], v118
	v_cvt_pk_f32_fp8_sdwa v[160:161], v118 src0_sel:WORD_1
	v_cvt_pk_f32_fp8_e32 v[164:165], v119
	v_cvt_pk_f32_fp8_e32 v[118:119], v120
	v_cvt_pk_f32_fp8_sdwa v[168:169], v120 src0_sel:WORD_1
	v_cvt_pk_f32_fp8_e32 v[170:171], v121
	v_cvt_pk_f32_fp8_sdwa v[120:121], v121 src0_sel:WORD_1
	v_cvt_pk_f32_fp8_sdwa v[176:177], v123 src0_sel:WORD_1
	v_pk_fma_f32 v[82:83], v[90:91], v[56:57], v[82:83] op_sel:[0,1,0] op_sel_hi:[1,1,1]
	v_pk_fma_f32 v[78:79], v[100:101], v[58:59], v[78:79] op_sel_hi:[1,0,1]
	v_pk_fma_f32 v[78:79], v[134:135], v[58:59], v[78:79] op_sel:[0,1,0] op_sel_hi:[1,1,1]
	v_pk_fma_f32 v[82:83], v[124:125], v[58:59], v[82:83] op_sel_hi:[1,0,1]
	v_pk_fma_f32 v[78:79], v[104:105], v[60:61], v[78:79] op_sel_hi:[1,0,1]
	v_pk_fma_f32 v[78:79], v[148:149], v[60:61], v[78:79] op_sel:[0,1,0] op_sel_hi:[1,1,1]
	v_pk_fma_f32 v[82:83], v[130:131], v[58:59], v[82:83] op_sel:[0,1,0] op_sel_hi:[1,1,1]
	v_pk_fma_f32 v[78:79], v[114:115], v[62:63], v[78:79] op_sel_hi:[1,0,1]
	v_pk_fma_f32 v[78:79], v[162:163], v[62:63], v[78:79] op_sel:[0,1,0] op_sel_hi:[1,1,1]
	v_pk_fma_f32 v[82:83], v[138:139], v[60:61], v[82:83] op_sel_hi:[1,0,1]
	v_cvt_pk_f32_fp8_e32 v[172:173], v122
	v_pk_fma_f32 v[78:79], v[120:121], v[54:55], v[78:79] op_sel_hi:[1,0,1]
	v_pk_fma_f32 v[82:83], v[144:145], v[60:61], v[82:83] op_sel:[0,1,0] op_sel_hi:[1,1,1]
	v_pk_fma_f32 v[124:125], v[176:177], v[54:55], v[78:79] op_sel:[0,1,0] op_sel_hi:[1,1,1]
	v_pk_fma_f32 v[82:83], v[152:153], v[62:63], v[82:83] op_sel_hi:[1,0,1]
	v_pk_fma_f32 v[82:83], v[158:159], v[62:63], v[82:83] op_sel:[0,1,0] op_sel_hi:[1,1,1]
	v_pk_fma_f32 v[82:83], v[118:119], v[54:55], v[82:83] op_sel_hi:[1,0,1]
	v_cvt_pk_f32_fp8_sdwa v[132:133], v102 src0_sel:WORD_1
	v_cvt_pk_f32_fp8_e32 v[102:103], v103
	v_pk_fma_f32 v[118:119], v[172:173], v[54:55], v[82:83] op_sel:[0,1,0] op_sel_hi:[1,1,1]
	v_pk_fma_f32 v[82:83], v[202:203], v[76:77], v[108:109] op_sel:[0,1,0] op_sel_hi:[1,1,1]
	v_pk_fma_f32 v[76:77], v[204:205], v[76:77], v[110:111] op_sel:[0,1,0] op_sel_hi:[1,1,1]
	v_pk_fma_f32 v[82:83], v[84:85], v[56:57], v[82:83] op_sel_hi:[1,0,1]
	v_pk_fma_f32 v[228:229], v[86:87], v[56:57], v[76:77] op_sel_hi:[1,0,1]
	v_cvt_pk_f32_fp8_sdwa v[146:147], v112 src0_sel:WORD_1
	v_cvt_pk_f32_fp8_e32 v[112:113], v113
	v_pk_fma_f32 v[228:229], v[96:97], v[56:57], v[228:229] op_sel:[0,1,0] op_sel_hi:[1,1,1]
	v_pk_fma_f32 v[82:83], v[92:93], v[56:57], v[82:83] op_sel:[0,1,0] op_sel_hi:[1,1,1]
	v_pk_fma_f32 v[228:229], v[128:129], v[58:59], v[228:229] op_sel_hi:[1,0,1]
	v_pk_fma_f32 v[82:83], v[126:127], v[58:59], v[82:83] op_sel_hi:[1,0,1]
	v_pk_fma_f32 v[228:229], v[102:103], v[58:59], v[228:229] op_sel:[0,1,0] op_sel_hi:[1,1,1]
	v_cvt_pk_f32_fp8_e32 v[178:179], v123
	v_pk_fma_f32 v[228:229], v[142:143], v[60:61], v[228:229] op_sel_hi:[1,0,1]
	v_pk_fma_f32 v[82:83], v[132:133], v[58:59], v[82:83] op_sel:[0,1,0] op_sel_hi:[1,1,1]
	v_pk_fma_f32 v[228:229], v[112:113], v[60:61], v[228:229] op_sel:[0,1,0] op_sel_hi:[1,1,1]
	v_pk_fma_f32 v[82:83], v[140:141], v[60:61], v[82:83] op_sel_hi:[1,0,1]
	v_pk_fma_f32 v[228:229], v[156:157], v[62:63], v[228:229] op_sel_hi:[1,0,1]
	v_pk_fma_f32 v[82:83], v[146:147], v[60:61], v[82:83] op_sel:[0,1,0] op_sel_hi:[1,1,1]
	v_pk_fma_f32 v[228:229], v[164:165], v[62:63], v[228:229] op_sel:[0,1,0] op_sel_hi:[1,1,1]
	v_pk_fma_f32 v[82:83], v[154:155], v[62:63], v[82:83] op_sel_hi:[1,0,1]
	v_pk_fma_f32 v[228:229], v[170:171], v[54:55], v[228:229] op_sel_hi:[1,0,1]
	v_pk_fma_f32 v[82:83], v[160:161], v[62:63], v[82:83] op_sel:[0,1,0] op_sel_hi:[1,1,1]
	v_pk_fma_f32 v[120:121], v[178:179], v[54:55], v[228:229] op_sel:[0,1,0] op_sel_hi:[1,1,1]
	v_cvt_pk_f32_fp8_sdwa v[174:175], v122 src0_sel:WORD_1
	v_pk_fma_f32 v[82:83], v[168:169], v[54:55], v[82:83] op_sel_hi:[1,0,1]
	v_pk_fma_f32 v[122:123], v[174:175], v[54:55], v[82:83] op_sel:[0,1,0] op_sel_hi:[1,1,1]
	s_setprio 0
	s_bitcmp0_b32 s17, 1
	s_cbranch_scc1 .LBB0_955
	s_lshl_b64 s[8:9], s[8:9], 17
	v_lshl_add_u64 v[54:55], v[0:1], 0, s[8:9]
	v_cvt_pk_bf16_f32 v9, v118, v119
	v_cvt_pk_bf16_f32 v11, v122, v123
	v_cvt_pk_bf16_f32 v13, v120, v121
	v_cvt_pk_bf16_f32 v15, v124, v125
	global_store_short v[54:55], v9, off
	global_store_short_d16_hi v[54:55], v9, off offset:128
	global_store_short v[54:55], v11, off offset:256
	global_store_short_d16_hi v[54:55], v11, off offset:384
	global_store_short v[54:55], v13, off offset:512
	global_store_short_d16_hi v[54:55], v13, off offset:640
	global_store_short v[54:55], v15, off offset:768
	global_store_short_d16_hi v[54:55], v15, off offset:896
	v_mov_b64_e32 v[118:119], 0
	v_mov_b64_e32 v[122:123], 0
	v_mov_b64_e32 v[120:121], 0
	v_mov_b64_e32 v[124:125], 0
	s_branch .LBB0_955
